# gemm_out: first eight residual loads of the epilogue issued before the K-loop's final barrier (exit path)
# speedup vs baseline: 1.0006x; 1.0006x over previous
; #define PG8_STAGE(bufoff, gbase, voff) do { _Pragma("unroll") for (int _i = 0; _i < 2; ++_i) \
;         __builtin_amdgcn_global_load_lds((const unsigned*)((const char*)(gbase) + (voff)[_i]), (LAS unsigned*)(lds + (bufoff) + ldsw + _i * 8192), 16, 0, 0); } while (0)
; #define PG8_LDA(dst, b, h) do { _Pragma("unroll") for (int m = 0; m < 4; ++m) _Pragma("unroll") for (int k = 0; k < 2; ++k) dst[m][k] = *(const LAS bf16x8*)(lds + PG8_SA(b, h) + aoff + m * 2048 + k * 1024); } while (0)
; #define PG8_LDB(dst, b, h) do { _Pragma("unroll") for (int n = 0; n < 2; ++n) _Pragma("unroll") for (int k = 0; k < 2; ++k) dst[n][k] = *(const LAS bf16x8*)(lds + PG8_SB(b, h) + boff + n * 2048 + k * 1024); } while (0)
; #define PG8_MMA(ai, bj, At, Bt) do { __builtin_amdgcn_s_setprio(1); _Pragma("unroll") for (int m = 0; m < 4; ++m) _Pragma("unroll") for (int n = 0; n < 2; ++n) _Pragma("unroll") for (int k = 0; k < 2; ++k) \
;         acc[ai][bj][m][n] = __builtin_amdgcn_mfma_f32_16x16x32_bf16(Bt[n][k], At[m][k], acc[ai][bj][m][n], 0, 0, 0); __builtin_amdgcn_s_setprio(0); } while (0)
; #define PG8_WAIT_V(n) asm volatile("s_waitcnt vmcnt(" #n ")" ::: "memory")
; #define PG8_WAIT_L(n) asm volatile("s_waitcnt lgkmcnt(" #n ")" ::: "memory")
; #define PG8_BAR __builtin_amdgcn_s_barrier()
; #define PG8_SCHED __builtin_amdgcn_sched_barrier(0)
; template <class Epi, class Sched>
; __device__ __forceinline__ void gemm_phase(LAS unsigned char* lds, const bf16_t* Abase, const int K, const Sched& S, const Epi& E, const int wvid) {
;     ...
;             PG8_LDB(B0, 0, 0); PG8_SCHED; PG8_LDA(At, 0, 0); PG8_STAGE(PG8_SA(1, 1), a1, voffA[1]);
;             PG8_WAIT_L(8); PG8_BAR; PG8_WAIT_L(0); PG8_MMA(0, 0, At, B0); PG8_BAR; PG8_SCHED;
;             if (last && has_next) PG8_AOFF(nxt);
;             const char* a2 = last ? Ab : Ab + (size_t)(t + 2) * kstep; const char* b2 = last ? nB : cB + (size_t)(t + 2) * kstep;
;             const char* a3 = a2 + kstep; const char* b3 = b2 + kstep;
;             PG8_LDB(B1, 0, 1); PG8_STAGE(PG8_SB(0, 0), b2, voffB);
;             PG8_BAR; PG8_WAIT_L(0); PG8_MMA(0, 1, At, B1); PG8_BAR;
;             PG8_LDA(At, 0, 1); PG8_STAGE(PG8_SA(0, 0), a2, voffA[0]);
;             PG8_BAR; PG8_WAIT_L(0); PG8_MMA(1, 0, At, B0); PG8_BAR; PG8_SCHED;
;             PG8_STAGE(PG8_SB(0, 1), b2 + hstep, voffB);
;             PG8_WAIT_V(6); PG8_BAR; PG8_MMA(1, 1, At, B1); PG8_BAR;
.LBB0_1005:
	s_add_i32 s60, s60, 2
	s_add_u32 s28, s26, 0x100
	s_addc_u32 s29, s27, 0
	s_and_b64 s[34:35], s[30:31], exec
	s_cselect_b32 s34, 0, s28
	s_cselect_b32 s35, 0, s29
	s_add_u32 s34, s0, s34
	s_addc_u32 s35, s1, s35
	s_add_u32 s61, s23, s26
	s_addc_u32 s62, s58, s27
	s_add_i32 s63, 0, 0x14000
	s_and_b64 s[26:27], s[30:31], exec
	s_cselect_b32 s27, s11, s62
	s_cselect_b32 s26, s17, s61
	s_mov_b32 m0, s43
	v_add_u32_e32 v183, s63, v194
	v_lshl_add_u64 v[224:225], s[26:27], 0, v[178:179]
	ds_read_b128 v[196:199], v183
	ds_read_b128 v[200:203], v183 offset:1024
	ds_read_b128 v[206:209], v183 offset:2048
	ds_read_b128 v[210:213], v183 offset:3072
	global_load_lds_dwordx4 v[224:225], off
	v_lshl_add_u64 v[226:227], s[26:27], 0, v[180:181]
	s_mov_b32 m0, s46
	s_nop 0
	global_load_lds_dwordx4 v[226:227], off
	s_barrier
	s_waitcnt lgkmcnt(0)
	s_waitcnt lgkmcnt(0)
	v_mfma_f32_16x16x32_bf16 v[94:97], v[196:199], v[170:173], v[94:97]
	v_mfma_f32_16x16x32_bf16 v[90:93], v[206:209], v[170:173], v[90:93]
	v_mfma_f32_16x16x32_bf16 v[86:89], v[196:199], v[162:165], v[86:89]
	v_mfma_f32_16x16x32_bf16 v[82:85], v[206:209], v[162:165], v[82:85]
	v_mfma_f32_16x16x32_bf16 v[78:81], v[196:199], v[154:157], v[78:81]
	v_mfma_f32_16x16x32_bf16 v[74:77], v[206:209], v[154:157], v[74:77]
	v_mfma_f32_16x16x32_bf16 v[70:73], v[196:199], v[146:149], v[70:73]
	v_mfma_f32_16x16x32_bf16 v[66:69], v[206:209], v[146:149], v[66:69]
	v_mfma_f32_16x16x32_bf16 v[94:97], v[200:203], v[174:177], v[94:97]
	v_mfma_f32_16x16x32_bf16 v[90:93], v[210:213], v[174:177], v[90:93]
	v_mfma_f32_16x16x32_bf16 v[86:89], v[200:203], v[166:169], v[86:89]
	v_mfma_f32_16x16x32_bf16 v[82:85], v[210:213], v[166:169], v[82:85]
	v_mfma_f32_16x16x32_bf16 v[78:81], v[200:203], v[158:161], v[78:81]
	v_mfma_f32_16x16x32_bf16 v[74:77], v[210:213], v[158:161], v[74:77]
	v_mfma_f32_16x16x32_bf16 v[70:73], v[200:203], v[150:153], v[70:73]
	v_mfma_f32_16x16x32_bf16 v[66:69], v[210:213], v[150:153], v[66:69]
	s_mov_b32 m0, s42
	s_barrier
	ds_read_b128 v[146:149], v195 offset:16384
	ds_read_b128 v[150:153], v195 offset:17408
	ds_read_b128 v[154:157], v195 offset:18432
	ds_read_b128 v[158:161], v195 offset:19456
	ds_read_b128 v[162:165], v195 offset:20480
	ds_read_b128 v[166:169], v195 offset:21504
	ds_read_b128 v[170:173], v195 offset:22528
	ds_read_b128 v[174:177], v195 offset:23552
	global_load_lds_dwordx4 v0, s[34:35]
	s_mov_b32 m0, s47
	v_mov_b32_e32 v185, v1
	global_load_lds_dwordx4 v184, s[34:35]
	s_barrier
	s_waitcnt lgkmcnt(0)
	v_lshl_add_u64 v[228:229], s[34:35], 0, v[0:1]
	v_lshl_add_u64 v[230:231], s[34:35], 0, v[184:185]
	s_waitcnt lgkmcnt(0)
	v_mfma_f32_16x16x32_bf16 v[62:65], v[130:133], v[146:149], v[62:65]
	v_mfma_f32_16x16x32_bf16 v[58:61], v[138:141], v[146:149], v[58:61]
	v_mfma_f32_16x16x32_bf16 v[54:57], v[130:133], v[154:157], v[54:57]
	v_mfma_f32_16x16x32_bf16 v[50:53], v[138:141], v[154:157], v[50:53]
	v_mfma_f32_16x16x32_bf16 v[42:45], v[130:133], v[162:165], v[42:45]
	v_mfma_f32_16x16x32_bf16 v[34:37], v[138:141], v[162:165], v[34:37]
	v_mfma_f32_16x16x32_bf16 v[26:29], v[130:133], v[170:173], v[26:29]
	v_mfma_f32_16x16x32_bf16 v[18:21], v[138:141], v[170:173], v[18:21]
	v_mfma_f32_16x16x32_bf16 v[62:65], v[134:137], v[150:153], v[62:65]
	v_mfma_f32_16x16x32_bf16 v[58:61], v[142:145], v[150:153], v[58:61]
	v_mfma_f32_16x16x32_bf16 v[54:57], v[134:137], v[158:161], v[54:57]
	v_mfma_f32_16x16x32_bf16 v[50:53], v[142:145], v[158:161], v[50:53]
	v_mfma_f32_16x16x32_bf16 v[42:45], v[134:137], v[166:169], v[42:45]
	v_mfma_f32_16x16x32_bf16 v[34:37], v[142:145], v[166:169], v[34:37]
	v_mfma_f32_16x16x32_bf16 v[26:29], v[134:137], v[174:177], v[26:29]
	v_mfma_f32_16x16x32_bf16 v[18:21], v[142:145], v[174:177], v[18:21]
	s_barrier
	s_add_u32 s30, s26, 0x40000
	s_addc_u32 s31, s27, 0
	s_add_i32 s61, s63, s40
	v_lshl_add_u64 v[130:131], s[30:31], 0, v[178:179]
	s_mov_b32 m0, s61
	s_nop 0
	global_load_lds_dwordx4 v[130:131], off
	v_lshl_add_u64 v[130:131], s[30:31], 0, v[180:181]
	s_add_i32 m0, s61, 0x2000
	s_nop 0
	global_load_lds_dwordx4 v[130:131], off
	s_waitcnt vmcnt(6)
	s_barrier
	v_mfma_f32_16x16x32_bf16 v[46:49], v[196:199], v[146:149], v[46:49]
	v_mfma_f32_16x16x32_bf16 v[38:41], v[206:209], v[146:149], v[38:41]
	v_mfma_f32_16x16x32_bf16 v[30:33], v[196:199], v[154:157], v[30:33]
	v_mfma_f32_16x16x32_bf16 v[22:25], v[206:209], v[154:157], v[22:25]
	v_mfma_f32_16x16x32_bf16 v[14:17], v[196:199], v[162:165], v[14:17]
	v_mfma_f32_16x16x32_bf16 v[10:13], v[206:209], v[162:165], v[10:13]
	v_mfma_f32_16x16x32_bf16 v[6:9], v[196:199], v[170:173], v[6:9]
	v_mfma_f32_16x16x32_bf16 v[2:5], v[206:209], v[170:173], v[2:5]
	v_mfma_f32_16x16x32_bf16 v[46:49], v[200:203], v[150:153], v[46:49]
	v_mfma_f32_16x16x32_bf16 v[38:41], v[210:213], v[150:153], v[38:41]
	v_mfma_f32_16x16x32_bf16 v[30:33], v[200:203], v[158:161], v[30:33]
	v_mfma_f32_16x16x32_bf16 v[22:25], v[210:213], v[158:161], v[22:25]
	v_mfma_f32_16x16x32_bf16 v[14:17], v[200:203], v[166:169], v[14:17]
	v_mfma_f32_16x16x32_bf16 v[10:13], v[210:213], v[166:169], v[10:13]
	v_mfma_f32_16x16x32_bf16 v[6:9], v[200:203], v[174:177], v[6:9]
	v_mfma_f32_16x16x32_bf16 v[2:5], v[210:213], v[174:177], v[2:5]
	s_add_i32 s30, 0, 0x18000
	v_add_u32_e32 v142, s30, v194
	s_barrier
; #define PG8_STAGE(bufoff, gbase, voff) do { _Pragma("unroll") for (int _i = 0; _i < 2; ++_i) \
;         __builtin_amdgcn_global_load_lds((const unsigned*)((const char*)(gbase) + (voff)[_i]), (LAS unsigned*)(lds + (bufoff) + ldsw + _i * 8192), 16, 0, 0); } while (0)
; #define PG8_LDA(dst, b, h) do { _Pragma("unroll") for (int m = 0; m < 4; ++m) _Pragma("unroll") for (int k = 0; k < 2; ++k) dst[m][k] = *(const LAS bf16x8*)(lds + PG8_SA(b, h) + aoff + m * 2048 + k * 1024); } while (0)
; #define PG8_LDB(dst, b, h) do { _Pragma("unroll") for (int n = 0; n < 2; ++n) _Pragma("unroll") for (int k = 0; k < 2; ++k) dst[n][k] = *(const LAS bf16x8*)(lds + PG8_SB(b, h) + boff + n * 2048 + k * 1024); } while (0)
; #define PG8_MMA(ai, bj, At, Bt) do { __builtin_amdgcn_s_setprio(1); _Pragma("unroll") for (int m = 0; m < 4; ++m) _Pragma("unroll") for (int n = 0; n < 2; ++n) _Pragma("unroll") for (int k = 0; k < 2; ++k) \
;         acc[ai][bj][m][n] = __builtin_amdgcn_mfma_f32_16x16x32_bf16(Bt[n][k], At[m][k], acc[ai][bj][m][n], 0, 0, 0); __builtin_amdgcn_s_setprio(0); } while (0)
; #define PG8_WAIT_V(n) asm volatile("s_waitcnt vmcnt(" #n ")" ::: "memory")
; #define PG8_WAIT_L(n) asm volatile("s_waitcnt lgkmcnt(" #n ")" ::: "memory")
; #define PG8_BAR __builtin_amdgcn_s_barrier()
; #define PG8_SCHED __builtin_amdgcn_sched_barrier(0)
; template <class Epi, class Sched>
; __device__ __forceinline__ void gemm_phase(LAS unsigned char* lds, const bf16_t* Abase, const int K, const Sched& S, const Epi& E, const int wvid) {
;     ...
;             PG8_LDB(B0, 1, 0); PG8_SCHED; PG8_LDA(At, 1, 0); PG8_STAGE(PG8_SA(0, 1), a2, voffA[1]);
;             PG8_WAIT_L(8); PG8_BAR; PG8_WAIT_L(0); PG8_MMA(0, 0, At, B0); PG8_BAR; PG8_SCHED;
;             PG8_LDB(B1, 1, 1); PG8_STAGE(PG8_SB(1, 0), b3, voffB);
;             PG8_BAR; PG8_WAIT_L(0); PG8_MMA(0, 1, At, B1); PG8_BAR;
;             PG8_LDA(At, 1, 1); PG8_STAGE(PG8_SA(1, 0), a3, voffA[0]);
;             PG8_BAR; PG8_WAIT_L(0); PG8_MMA(1, 0, At, B0); PG8_BAR; PG8_SCHED;
;             PG8_STAGE(PG8_SB(1, 1), b3 + hstep, voffB);
;             PG8_WAIT_V(6); PG8_BAR; PG8_MMA(1, 1, At, B1); PG8_BAR;
;         }
	ds_read_b128 v[130:133], v142
	ds_read_b128 v[134:137], v142 offset:1024
	ds_read_b128 v[138:141], v142 offset:2048
	ds_read_b128 v[142:145], v142 offset:3072
	s_mov_b32 m0, s48
	v_lshl_add_u64 v[192:193], s[34:35], 0, v[192:193]
	ds_read_b128 v[146:149], v195 offset:32768
	ds_read_b128 v[150:153], v195 offset:33792
	ds_read_b128 v[154:157], v195 offset:34816
	ds_read_b128 v[158:161], v195 offset:35840
	ds_read_b128 v[162:165], v195 offset:36864
	ds_read_b128 v[166:169], v195 offset:37888
	ds_read_b128 v[170:173], v195 offset:38912
	ds_read_b128 v[174:177], v195 offset:39936
	global_load_lds_dwordx4 v[192:193], off
	v_lshl_add_u64 v[192:193], s[34:35], 0, v[186:187]
	s_mov_b32 m0, s49
	s_nop 0
	global_load_lds_dwordx4 v[192:193], off
	s_waitcnt lgkmcnt(8)
	s_barrier
	s_waitcnt lgkmcnt(0)
	s_waitcnt lgkmcnt(0)
	v_mfma_f32_16x16x32_bf16 v[126:129], v[130:133], v[146:149], v[126:129]
	v_mfma_f32_16x16x32_bf16 v[122:125], v[138:141], v[146:149], v[122:125]
	v_mfma_f32_16x16x32_bf16 v[118:121], v[130:133], v[154:157], v[118:121]
	v_mfma_f32_16x16x32_bf16 v[114:117], v[138:141], v[154:157], v[114:117]
	v_mfma_f32_16x16x32_bf16 v[110:113], v[130:133], v[162:165], v[110:113]
	v_mfma_f32_16x16x32_bf16 v[106:109], v[138:141], v[162:165], v[106:109]
	v_mfma_f32_16x16x32_bf16 v[102:105], v[130:133], v[170:173], v[102:105]
	v_mfma_f32_16x16x32_bf16 v[98:101], v[138:141], v[170:173], v[98:101]
	v_mfma_f32_16x16x32_bf16 v[126:129], v[134:137], v[150:153], v[126:129]
	v_mfma_f32_16x16x32_bf16 v[122:125], v[142:145], v[150:153], v[122:125]
	v_mfma_f32_16x16x32_bf16 v[118:121], v[134:137], v[158:161], v[118:121]
	v_mfma_f32_16x16x32_bf16 v[114:117], v[142:145], v[158:161], v[114:117]
	v_mfma_f32_16x16x32_bf16 v[110:113], v[134:137], v[166:169], v[110:113]
	v_mfma_f32_16x16x32_bf16 v[106:109], v[142:145], v[166:169], v[106:109]
	v_mfma_f32_16x16x32_bf16 v[102:105], v[134:137], v[174:177], v[102:105]
	v_mfma_f32_16x16x32_bf16 v[98:101], v[142:145], v[174:177], v[98:101]
	s_barrier
	s_add_i32 s31, 0, 0x1c000
	s_add_i32 s30, s30, s40
	v_add_u32_e32 v183, s31, v194
	v_lshl_add_u64 v[192:193], v[224:225], 0, s[12:13]
	s_mov_b32 m0, s30
	ds_read_b128 v[196:199], v183
	ds_read_b128 v[200:203], v183 offset:1024
	ds_read_b128 v[206:209], v183 offset:2048
	ds_read_b128 v[210:213], v183 offset:3072
	global_load_lds_dwordx4 v[192:193], off
	v_lshl_add_u64 v[192:193], v[226:227], 0, s[12:13]
	s_add_i32 m0, s30, 0x2000
	s_nop 0
	global_load_lds_dwordx4 v[192:193], off
	s_barrier
	s_waitcnt lgkmcnt(0)
	s_waitcnt lgkmcnt(0)
	v_mfma_f32_16x16x32_bf16 v[94:97], v[196:199], v[146:149], v[94:97]
	v_mfma_f32_16x16x32_bf16 v[90:93], v[206:209], v[146:149], v[90:93]
	v_mfma_f32_16x16x32_bf16 v[86:89], v[196:199], v[154:157], v[86:89]
	v_mfma_f32_16x16x32_bf16 v[82:85], v[206:209], v[154:157], v[82:85]
	v_mfma_f32_16x16x32_bf16 v[78:81], v[196:199], v[162:165], v[78:81]
	v_mfma_f32_16x16x32_bf16 v[74:77], v[206:209], v[162:165], v[74:77]
	v_mfma_f32_16x16x32_bf16 v[70:73], v[196:199], v[170:173], v[70:73]
	v_mfma_f32_16x16x32_bf16 v[66:69], v[206:209], v[170:173], v[66:69]
	v_mfma_f32_16x16x32_bf16 v[94:97], v[200:203], v[150:153], v[94:97]
	v_mfma_f32_16x16x32_bf16 v[90:93], v[210:213], v[150:153], v[90:93]
	v_mfma_f32_16x16x32_bf16 v[86:89], v[200:203], v[158:161], v[86:89]
	v_mfma_f32_16x16x32_bf16 v[82:85], v[210:213], v[158:161], v[82:85]
	v_mfma_f32_16x16x32_bf16 v[78:81], v[200:203], v[166:169], v[78:81]
	v_mfma_f32_16x16x32_bf16 v[74:77], v[210:213], v[166:169], v[74:77]
	v_mfma_f32_16x16x32_bf16 v[70:73], v[200:203], v[174:177], v[70:73]
	v_mfma_f32_16x16x32_bf16 v[66:69], v[210:213], v[174:177], v[66:69]
	s_mov_b32 m0, s51
	v_lshl_add_u64 v[192:193], v[228:229], 0, s[12:13]
	s_barrier
	ds_read_b128 v[146:149], v195 offset:49152
	ds_read_b128 v[150:153], v195 offset:50176
	ds_read_b128 v[154:157], v195 offset:51200
	ds_read_b128 v[158:161], v195 offset:52224
	ds_read_b128 v[162:165], v195 offset:53248
	ds_read_b128 v[166:169], v195 offset:54272
	ds_read_b128 v[170:173], v195 offset:55296
	ds_read_b128 v[174:177], v195 offset:56320
	global_load_lds_dwordx4 v[192:193], off
	v_lshl_add_u64 v[192:193], v[230:231], 0, s[12:13]
	s_mov_b32 m0, s52
	s_nop 0
	global_load_lds_dwordx4 v[192:193], off
	s_barrier
	s_waitcnt lgkmcnt(0)
	s_waitcnt lgkmcnt(0)
	v_mfma_f32_16x16x32_bf16 v[62:65], v[130:133], v[146:149], v[62:65]
	v_mfma_f32_16x16x32_bf16 v[58:61], v[138:141], v[146:149], v[58:61]
	v_mfma_f32_16x16x32_bf16 v[54:57], v[130:133], v[154:157], v[54:57]
	v_mfma_f32_16x16x32_bf16 v[50:53], v[138:141], v[154:157], v[50:53]
	v_mfma_f32_16x16x32_bf16 v[42:45], v[130:133], v[162:165], v[42:45]
	v_mfma_f32_16x16x32_bf16 v[34:37], v[138:141], v[162:165], v[34:37]
	v_mfma_f32_16x16x32_bf16 v[26:29], v[130:133], v[170:173], v[26:29]
	v_mfma_f32_16x16x32_bf16 v[18:21], v[138:141], v[170:173], v[18:21]
	v_mfma_f32_16x16x32_bf16 v[62:65], v[134:137], v[150:153], v[62:65]
	v_mfma_f32_16x16x32_bf16 v[58:61], v[142:145], v[150:153], v[58:61]
	v_mfma_f32_16x16x32_bf16 v[54:57], v[134:137], v[158:161], v[54:57]
	v_mfma_f32_16x16x32_bf16 v[50:53], v[142:145], v[158:161], v[50:53]
	v_mfma_f32_16x16x32_bf16 v[42:45], v[134:137], v[166:169], v[42:45]
	v_mfma_f32_16x16x32_bf16 v[34:37], v[142:145], v[166:169], v[34:37]
	v_mfma_f32_16x16x32_bf16 v[26:29], v[134:137], v[174:177], v[26:29]
	v_mfma_f32_16x16x32_bf16 v[18:21], v[142:145], v[174:177], v[18:21]
	s_barrier
	s_add_u32 s26, s26, 0x40080
	s_addc_u32 s27, s27, 0
	s_add_i32 s30, s31, s40
	v_lshl_add_u64 v[130:131], s[26:27], 0, v[178:179]
	s_mov_b32 m0, s30
	s_nop 0
	global_load_lds_dwordx4 v[130:131], off
	v_lshl_add_u64 v[130:131], s[26:27], 0, v[180:181]
	s_add_i32 m0, s30, 0x2000
	s_nop 0
	global_load_lds_dwordx4 v[130:131], off
	s_waitcnt vmcnt(6)
	s_barrier
	v_mfma_f32_16x16x32_bf16 v[46:49], v[196:199], v[146:149], v[46:49]
	v_mfma_f32_16x16x32_bf16 v[38:41], v[206:209], v[146:149], v[38:41]
	v_mfma_f32_16x16x32_bf16 v[30:33], v[196:199], v[154:157], v[30:33]
	v_mfma_f32_16x16x32_bf16 v[22:25], v[206:209], v[154:157], v[22:25]
	v_mfma_f32_16x16x32_bf16 v[14:17], v[196:199], v[162:165], v[14:17]
	v_mfma_f32_16x16x32_bf16 v[10:13], v[206:209], v[162:165], v[10:13]
	v_mfma_f32_16x16x32_bf16 v[6:9], v[196:199], v[170:173], v[6:9]
	v_mfma_f32_16x16x32_bf16 v[2:5], v[206:209], v[170:173], v[2:5]
	v_mfma_f32_16x16x32_bf16 v[46:49], v[200:203], v[150:153], v[46:49]
	v_mfma_f32_16x16x32_bf16 v[38:41], v[210:213], v[150:153], v[38:41]
	v_mfma_f32_16x16x32_bf16 v[30:33], v[200:203], v[158:161], v[30:33]
	v_mfma_f32_16x16x32_bf16 v[22:25], v[210:213], v[158:161], v[22:25]
	v_mfma_f32_16x16x32_bf16 v[14:17], v[200:203], v[166:169], v[14:17]
	v_mfma_f32_16x16x32_bf16 v[10:13], v[210:213], v[166:169], v[10:13]
	v_mfma_f32_16x16x32_bf16 v[6:9], v[200:203], v[174:177], v[6:9]
	v_mfma_f32_16x16x32_bf16 v[2:5], v[210:213], v[174:177], v[2:5]
	s_cmp_ge_i32 s60, s57
	s_cbranch_scc1 .LBB0_1007
	s_barrier
	s_mov_b64 s[26:27], s[28:29]
	s_branch .LBB0_1002
; __device__ __forceinline__ float bflo(unsigned w) { return __uint_as_float(w << 16); }
; __device__ __forceinline__ float bfhi(unsigned w) { return __uint_as_float(w & 0xFFFF0000u); }
; __device__ __forceinline__ unsigned cvt_pk_bf16(float lo, float hi) { f32x2c v = {lo, hi}; bf16x2c b = __builtin_convertvector(v, bf16x2c); return __builtin_bit_cast(unsigned, b); }
;     __device__ __forceinline__ void operator()(const f32x4 (&acc)[2][2][4][2], const Unit& u, int wr, int wc, int fr, int fq) const {
;         const int row0 = u.row0 + wr * 64 + fr, col0 = u.pn * BM + wc * 32 + 8 * fq;
;         if (u.kt * BK < Kfull) {
;             float* zp = ZP + ((size_t)u.e * BM + (wr * 64 + fr)) * D + col0;
; #pragma unroll
;             for (int ai = 0; ai < 2; ++ai)
; #pragma unroll
;                 for (int m = 0; m < 4; ++m)
; #pragma unroll
;                     for (int bj = 0; bj < 2; ++bj) { float* q = zp + (size_t)(ai * HALF + m * 16) * D + bj * HALF; *(f32x4*)q = acc[ai][bj][m][0]; *(f32x4*)(q + 4) = acc[ai][bj][m][1]; }
;             return;
;         }
; #pragma unroll
;         for (int ai = 0; ai < 2; ++ai)
; #pragma unroll
;             for (int m = 0; m < 4; ++m) { const size_t ro = (size_t)(row0 + ai * HALF + m * 16) * D + col0;
; #pragma unroll
;                 for (int bj = 0; bj < 2; ++bj) { const u32x4 h = *(const u32x4*)(hb + ro + bj * HALF); const f32x4 v0 = acc[ai][bj][m][0], v1 = acc[ai][bj][m][1];
;                     u32x4 w; w.x = cvt_pk_bf16(v0[0] + ALPHA * bflo(h.x), v0[1] + ALPHA * bfhi(h.x)); w.y = cvt_pk_bf16(v0[2] + ALPHA * bflo(h.y), v0[3] + ALPHA * bfhi(h.y));
;                     w.z = cvt_pk_bf16(v1[0] + ALPHA * bflo(h.z), v1[1] + ALPHA * bfhi(h.z)); w.w = cvt_pk_bf16(v1[2] + ALPHA * bflo(h.w), v1[3] + ALPHA * bfhi(h.w));
;                     *(u32x4*)(Z + ro + bj * HALF) = w; } }
.LBB0_1007:
	v_lshl_or_b32 v130, s22, 8, v189
	s_mov_b64 s[22:23], -1
	s_cmp_lt_i32 s57, 16
	v_ashrrev_i32_e32 v131, 31, v130
	s_cbranch_scc1 .Lgo_ks
	v_add_u32_e32 v132, s9, v188
	v_ashrrev_i32_e32 v133, 31, v132
	v_lshlrev_b64 v[132:133], 10, v[132:133]
	v_lshl_add_u64 v[132:133], v[132:133], 0, v[130:131]
	v_lshlrev_b64 v[132:133], 1, v[132:133]
	v_lshl_add_u64 v[138:139], s[4:5], 0, v[132:133]
	v_lshl_add_u64 v[140:141], s[2:3], 0, v[132:133]
	v_mov_b64_e32 v[142:143], v[138:139]
	global_load_dwordx4 v[144:147], v[142:143], off
	global_load_dwordx4 v[148:151], v[142:143], off offset:256
	v_add_co_u32_e32 v142, vcc, 0x8000, v142
	s_nop 1
	v_addc_co_u32_e32 v143, vcc, 0, v143, vcc
	global_load_dwordx4 v[152:155], v[142:143], off
	global_load_dwordx4 v[156:159], v[142:143], off offset:256
	v_add_co_u32_e32 v142, vcc, 0x8000, v142
	s_nop 1
	v_addc_co_u32_e32 v143, vcc, 0, v143, vcc
	global_load_dwordx4 v[160:163], v[142:143], off
	global_load_dwordx4 v[164:167], v[142:143], off offset:256
	v_add_co_u32_e32 v142, vcc, 0x8000, v142
	s_nop 1
	v_addc_co_u32_e32 v143, vcc, 0, v143, vcc
	global_load_dwordx4 v[168:171], v[142:143], off
	global_load_dwordx4 v[172:175], v[142:143], off offset:256
	v_add_co_u32_e32 v142, vcc, 0x28000, v142
	s_nop 1
	v_addc_co_u32_e32 v143, vcc, 0, v143, vcc
	s_barrier
	s_waitcnt vmcnt(7)
	v_lshlrev_b32_e32 v134, 16, v144
	v_and_b32_e32 v135, 0xffff0000, v144
	v_pk_fma_f32 v[134:135], v[134:135], s[88:89], v[126:127] op_sel_hi:[1,0,1]
	s_nop 0
	v_cvt_pk_bf16_f32 v144, v134, v135
	v_lshlrev_b32_e32 v134, 16, v145
	v_and_b32_e32 v135, 0xffff0000, v145
	v_pk_fma_f32 v[134:135], v[134:135], s[88:89], v[128:129] op_sel_hi:[1,0,1]
	s_nop 0
	v_cvt_pk_bf16_f32 v145, v134, v135
	v_lshlrev_b32_e32 v134, 16, v146
	v_and_b32_e32 v135, 0xffff0000, v146
	v_pk_fma_f32 v[134:135], v[134:135], s[88:89], v[122:123] op_sel_hi:[1,0,1]
	s_nop 0
	v_cvt_pk_bf16_f32 v146, v134, v135
	v_lshlrev_b32_e32 v134, 16, v147
	v_and_b32_e32 v135, 0xffff0000, v147
	v_pk_fma_f32 v[134:135], v[134:135], s[88:89], v[124:125] op_sel_hi:[1,0,1]
	s_nop 0
	v_cvt_pk_bf16_f32 v147, v134, v135
	global_store_dwordx4 v[140:141], v[144:147], off
	s_nop 1
	global_load_dwordx4 v[144:147], v[142:143], off
	s_waitcnt vmcnt(8)
	v_lshlrev_b32_e32 v134, 16, v148
	v_and_b32_e32 v135, 0xffff0000, v148
	v_pk_fma_f32 v[134:135], v[134:135], s[88:89], v[94:95] op_sel_hi:[1,0,1]
	s_nop 0
	v_cvt_pk_bf16_f32 v148, v134, v135
	v_lshlrev_b32_e32 v134, 16, v149
	v_and_b32_e32 v135, 0xffff0000, v149
	v_pk_fma_f32 v[134:135], v[134:135], s[88:89], v[96:97] op_sel_hi:[1,0,1]
	s_nop 0
	v_cvt_pk_bf16_f32 v149, v134, v135
	v_lshlrev_b32_e32 v134, 16, v150
	v_and_b32_e32 v135, 0xffff0000, v150
	v_pk_fma_f32 v[134:135], v[134:135], s[88:89], v[90:91] op_sel_hi:[1,0,1]
	s_nop 0
	v_cvt_pk_bf16_f32 v150, v134, v135
	v_lshlrev_b32_e32 v134, 16, v151
	v_and_b32_e32 v135, 0xffff0000, v151
	v_pk_fma_f32 v[134:135], v[134:135], s[88:89], v[92:93] op_sel_hi:[1,0,1]
	s_nop 0
	v_cvt_pk_bf16_f32 v151, v134, v135
	global_store_dwordx4 v[140:141], v[148:151], off offset:256
	v_add_co_u32_e32 v140, vcc, 0x8000, v140
	s_nop 1
	v_addc_co_u32_e32 v141, vcc, 0, v141, vcc
	global_load_dwordx4 v[148:151], v[142:143], off offset:256
	v_add_co_u32_e32 v142, vcc, 0x8000, v142
	s_nop 1
	v_addc_co_u32_e32 v143, vcc, 0, v143, vcc
	s_waitcnt vmcnt(9)
	v_lshlrev_b32_e32 v134, 16, v152
	v_and_b32_e32 v135, 0xffff0000, v152
	v_pk_fma_f32 v[134:135], v[134:135], s[88:89], v[118:119] op_sel_hi:[1,0,1]
	s_nop 0
	v_cvt_pk_bf16_f32 v152, v134, v135
	v_lshlrev_b32_e32 v134, 16, v153
	v_and_b32_e32 v135, 0xffff0000, v153
	v_pk_fma_f32 v[134:135], v[134:135], s[88:89], v[120:121] op_sel_hi:[1,0,1]
	s_nop 0
	v_cvt_pk_bf16_f32 v153, v134, v135
	v_lshlrev_b32_e32 v134, 16, v154
	v_and_b32_e32 v135, 0xffff0000, v154
	v_pk_fma_f32 v[134:135], v[134:135], s[88:89], v[114:115] op_sel_hi:[1,0,1]
	s_nop 0
	v_cvt_pk_bf16_f32 v154, v134, v135
	v_lshlrev_b32_e32 v134, 16, v155
	v_and_b32_e32 v135, 0xffff0000, v155
	v_pk_fma_f32 v[134:135], v[134:135], s[88:89], v[116:117] op_sel_hi:[1,0,1]
	s_nop 0
	v_cvt_pk_bf16_f32 v155, v134, v135
	global_store_dwordx4 v[140:141], v[152:155], off
	s_nop 1
	global_load_dwordx4 v[152:155], v[142:143], off
	s_waitcnt vmcnt(10)
	v_lshlrev_b32_e32 v134, 16, v156
	v_and_b32_e32 v135, 0xffff0000, v156
	v_pk_fma_f32 v[134:135], v[134:135], s[88:89], v[86:87] op_sel_hi:[1,0,1]
	s_nop 0
	v_cvt_pk_bf16_f32 v156, v134, v135
	v_lshlrev_b32_e32 v134, 16, v157
	v_and_b32_e32 v135, 0xffff0000, v157
	v_pk_fma_f32 v[134:135], v[134:135], s[88:89], v[88:89] op_sel_hi:[1,0,1]
	s_nop 0
	v_cvt_pk_bf16_f32 v157, v134, v135
	v_lshlrev_b32_e32 v134, 16, v158
	v_and_b32_e32 v135, 0xffff0000, v158
	v_pk_fma_f32 v[134:135], v[134:135], s[88:89], v[82:83] op_sel_hi:[1,0,1]
	s_nop 0
	v_cvt_pk_bf16_f32 v158, v134, v135
	v_lshlrev_b32_e32 v134, 16, v159
	v_and_b32_e32 v135, 0xffff0000, v159
	v_pk_fma_f32 v[134:135], v[134:135], s[88:89], v[84:85] op_sel_hi:[1,0,1]
	s_nop 0
	v_cvt_pk_bf16_f32 v159, v134, v135
	global_store_dwordx4 v[140:141], v[156:159], off offset:256
	v_add_co_u32_e32 v140, vcc, 0x8000, v140
	s_nop 1
	v_addc_co_u32_e32 v141, vcc, 0, v141, vcc
	global_load_dwordx4 v[156:159], v[142:143], off offset:256
	v_add_co_u32_e32 v142, vcc, 0x8000, v142
	s_nop 1
	v_addc_co_u32_e32 v143, vcc, 0, v143, vcc
	s_waitcnt vmcnt(11)
; __device__ __forceinline__ float bflo(unsigned w) { return __uint_as_float(w << 16); }
; __device__ __forceinline__ float bfhi(unsigned w) { return __uint_as_float(w & 0xFFFF0000u); }
; __device__ __forceinline__ unsigned cvt_pk_bf16(float lo, float hi) { f32x2c v = {lo, hi}; bf16x2c b = __builtin_convertvector(v, bf16x2c); return __builtin_bit_cast(unsigned, b); }
;     __device__ __forceinline__ void operator()(const f32x4 (&acc)[2][2][4][2], const Unit& u, int wr, int wc, int fr, int fq) const {
;     ...
;         for (int ai = 0; ai < 2; ++ai)
; #pragma unroll
;             for (int m = 0; m < 4; ++m) { const size_t ro = (size_t)(row0 + ai * HALF + m * 16) * D + col0;
; #pragma unroll
;                 for (int bj = 0; bj < 2; ++bj) { const u32x4 h = *(const u32x4*)(hb + ro + bj * HALF); const f32x4 v0 = acc[ai][bj][m][0], v1 = acc[ai][bj][m][1];
;                     u32x4 w; w.x = cvt_pk_bf16(v0[0] + ALPHA * bflo(h.x), v0[1] + ALPHA * bfhi(h.x)); w.y = cvt_pk_bf16(v0[2] + ALPHA * bflo(h.y), v0[3] + ALPHA * bfhi(h.y));
;                     w.z = cvt_pk_bf16(v1[0] + ALPHA * bflo(h.z), v1[1] + ALPHA * bfhi(h.z)); w.w = cvt_pk_bf16(v1[2] + ALPHA * bflo(h.w), v1[3] + ALPHA * bfhi(h.w));
;                     *(u32x4*)(Z + ro + bj * HALF) = w; } }
	v_lshlrev_b32_e32 v134, 16, v160
	v_and_b32_e32 v135, 0xffff0000, v160
	v_pk_fma_f32 v[134:135], v[134:135], s[88:89], v[110:111] op_sel_hi:[1,0,1]
	s_nop 0
	v_cvt_pk_bf16_f32 v160, v134, v135
	v_lshlrev_b32_e32 v134, 16, v161
	v_and_b32_e32 v135, 0xffff0000, v161
	v_pk_fma_f32 v[134:135], v[134:135], s[88:89], v[112:113] op_sel_hi:[1,0,1]
	s_nop 0
	v_cvt_pk_bf16_f32 v161, v134, v135
	v_lshlrev_b32_e32 v134, 16, v162
	v_and_b32_e32 v135, 0xffff0000, v162
	v_pk_fma_f32 v[134:135], v[134:135], s[88:89], v[106:107] op_sel_hi:[1,0,1]
	s_nop 0
	v_cvt_pk_bf16_f32 v162, v134, v135
	v_lshlrev_b32_e32 v134, 16, v163
	v_and_b32_e32 v135, 0xffff0000, v163
	v_pk_fma_f32 v[134:135], v[134:135], s[88:89], v[108:109] op_sel_hi:[1,0,1]
	s_nop 0
	v_cvt_pk_bf16_f32 v163, v134, v135
	global_store_dwordx4 v[140:141], v[160:163], off
	s_nop 1
	global_load_dwordx4 v[160:163], v[142:143], off
	s_waitcnt vmcnt(12)
	v_lshlrev_b32_e32 v134, 16, v164
	v_and_b32_e32 v135, 0xffff0000, v164
	v_pk_fma_f32 v[134:135], v[134:135], s[88:89], v[78:79] op_sel_hi:[1,0,1]
	s_nop 0
	v_cvt_pk_bf16_f32 v164, v134, v135
	v_lshlrev_b32_e32 v134, 16, v165
	v_and_b32_e32 v135, 0xffff0000, v165
	v_pk_fma_f32 v[134:135], v[134:135], s[88:89], v[80:81] op_sel_hi:[1,0,1]
	s_nop 0
	v_cvt_pk_bf16_f32 v165, v134, v135
	v_lshlrev_b32_e32 v134, 16, v166
	v_and_b32_e32 v135, 0xffff0000, v166
	v_pk_fma_f32 v[134:135], v[134:135], s[88:89], v[74:75] op_sel_hi:[1,0,1]
	s_nop 0
	v_cvt_pk_bf16_f32 v166, v134, v135
	v_lshlrev_b32_e32 v134, 16, v167
	v_and_b32_e32 v135, 0xffff0000, v167
	v_pk_fma_f32 v[134:135], v[134:135], s[88:89], v[76:77] op_sel_hi:[1,0,1]
	s_nop 0
	v_cvt_pk_bf16_f32 v167, v134, v135
	global_store_dwordx4 v[140:141], v[164:167], off offset:256
	v_add_co_u32_e32 v140, vcc, 0x8000, v140
	s_nop 1
	v_addc_co_u32_e32 v141, vcc, 0, v141, vcc
	global_load_dwordx4 v[164:167], v[142:143], off offset:256
	v_add_co_u32_e32 v142, vcc, 0x8000, v142
	s_nop 1
	v_addc_co_u32_e32 v143, vcc, 0, v143, vcc
	s_waitcnt vmcnt(13)
	v_lshlrev_b32_e32 v134, 16, v168
	v_and_b32_e32 v135, 0xffff0000, v168
	v_pk_fma_f32 v[134:135], v[134:135], s[88:89], v[102:103] op_sel_hi:[1,0,1]
	s_nop 0
	v_cvt_pk_bf16_f32 v168, v134, v135
	v_lshlrev_b32_e32 v134, 16, v169
	v_and_b32_e32 v135, 0xffff0000, v169
	v_pk_fma_f32 v[134:135], v[134:135], s[88:89], v[104:105] op_sel_hi:[1,0,1]
	s_nop 0
	v_cvt_pk_bf16_f32 v169, v134, v135
	v_lshlrev_b32_e32 v134, 16, v170
	v_and_b32_e32 v135, 0xffff0000, v170
	v_pk_fma_f32 v[134:135], v[134:135], s[88:89], v[98:99] op_sel_hi:[1,0,1]
	s_nop 0
	v_cvt_pk_bf16_f32 v170, v134, v135
	v_lshlrev_b32_e32 v134, 16, v171
	v_and_b32_e32 v135, 0xffff0000, v171
	v_pk_fma_f32 v[134:135], v[134:135], s[88:89], v[100:101] op_sel_hi:[1,0,1]
	s_nop 0
	v_cvt_pk_bf16_f32 v171, v134, v135
	global_store_dwordx4 v[140:141], v[168:171], off
	s_nop 1
	global_load_dwordx4 v[168:171], v[142:143], off
	s_waitcnt vmcnt(14)
	v_lshlrev_b32_e32 v134, 16, v172
	v_and_b32_e32 v135, 0xffff0000, v172
	v_pk_fma_f32 v[134:135], v[134:135], s[88:89], v[70:71] op_sel_hi:[1,0,1]
	s_nop 0
	v_cvt_pk_bf16_f32 v172, v134, v135
	v_lshlrev_b32_e32 v134, 16, v173
	v_and_b32_e32 v135, 0xffff0000, v173
	v_pk_fma_f32 v[134:135], v[134:135], s[88:89], v[72:73] op_sel_hi:[1,0,1]
	s_nop 0
	v_cvt_pk_bf16_f32 v173, v134, v135
	v_lshlrev_b32_e32 v134, 16, v174
	v_and_b32_e32 v135, 0xffff0000, v174
	v_pk_fma_f32 v[134:135], v[134:135], s[88:89], v[66:67] op_sel_hi:[1,0,1]
	s_nop 0
	v_cvt_pk_bf16_f32 v174, v134, v135
	v_lshlrev_b32_e32 v134, 16, v175
	v_and_b32_e32 v135, 0xffff0000, v175
	v_pk_fma_f32 v[134:135], v[134:135], s[88:89], v[68:69] op_sel_hi:[1,0,1]
	s_nop 0
	v_cvt_pk_bf16_f32 v175, v134, v135
	global_store_dwordx4 v[140:141], v[172:175], off offset:256
	v_add_co_u32_e32 v140, vcc, 0x28000, v140
	s_nop 1
	v_addc_co_u32_e32 v141, vcc, 0, v141, vcc
	global_load_dwordx4 v[172:175], v[142:143], off offset:256
	s_waitcnt vmcnt(14)
	v_lshlrev_b32_e32 v134, 16, v144
	v_and_b32_e32 v135, 0xffff0000, v144
	v_pk_fma_f32 v[134:135], v[134:135], s[88:89], v[62:63] op_sel_hi:[1,0,1]
	s_nop 0
	v_cvt_pk_bf16_f32 v144, v134, v135
	v_lshlrev_b32_e32 v134, 16, v145
	v_and_b32_e32 v135, 0xffff0000, v145
	v_pk_fma_f32 v[134:135], v[134:135], s[88:89], v[64:65] op_sel_hi:[1,0,1]
	s_nop 0
	v_cvt_pk_bf16_f32 v145, v134, v135
	v_lshlrev_b32_e32 v134, 16, v146
	v_and_b32_e32 v135, 0xffff0000, v146
	v_pk_fma_f32 v[134:135], v[134:135], s[88:89], v[58:59] op_sel_hi:[1,0,1]
	s_nop 0
	v_cvt_pk_bf16_f32 v146, v134, v135
	v_lshlrev_b32_e32 v134, 16, v147
	v_and_b32_e32 v135, 0xffff0000, v147
	v_pk_fma_f32 v[134:135], v[134:135], s[88:89], v[60:61] op_sel_hi:[1,0,1]
	s_nop 0
	v_cvt_pk_bf16_f32 v147, v134, v135
	global_store_dwordx4 v[140:141], v[144:147], off
	s_nop 1
	s_waitcnt vmcnt(13)
	v_lshlrev_b32_e32 v134, 16, v148
	v_and_b32_e32 v135, 0xffff0000, v148
	v_pk_fma_f32 v[134:135], v[134:135], s[88:89], v[46:47] op_sel_hi:[1,0,1]
	s_nop 0
	v_cvt_pk_bf16_f32 v148, v134, v135
	v_lshlrev_b32_e32 v134, 16, v149
	v_and_b32_e32 v135, 0xffff0000, v149
	v_pk_fma_f32 v[134:135], v[134:135], s[88:89], v[48:49] op_sel_hi:[1,0,1]
	s_nop 0
	v_cvt_pk_bf16_f32 v149, v134, v135
	v_lshlrev_b32_e32 v134, 16, v150
	v_and_b32_e32 v135, 0xffff0000, v150
	v_pk_fma_f32 v[134:135], v[134:135], s[88:89], v[38:39] op_sel_hi:[1,0,1]
	s_nop 0
	v_cvt_pk_bf16_f32 v150, v134, v135
	v_lshlrev_b32_e32 v134, 16, v151
	v_and_b32_e32 v135, 0xffff0000, v151
	v_pk_fma_f32 v[134:135], v[134:135], s[88:89], v[40:41] op_sel_hi:[1,0,1]
	s_nop 0
	v_cvt_pk_bf16_f32 v151, v134, v135
	global_store_dwordx4 v[140:141], v[148:151], off offset:256
	v_add_co_u32_e32 v140, vcc, 0x8000, v140
	s_nop 1
	v_addc_co_u32_e32 v141, vcc, 0, v141, vcc
	s_waitcnt vmcnt(12)
; __device__ __forceinline__ float bflo(unsigned w) { return __uint_as_float(w << 16); }
; __device__ __forceinline__ float bfhi(unsigned w) { return __uint_as_float(w & 0xFFFF0000u); }
; __device__ __forceinline__ unsigned cvt_pk_bf16(float lo, float hi) { f32x2c v = {lo, hi}; bf16x2c b = __builtin_convertvector(v, bf16x2c); return __builtin_bit_cast(unsigned, b); }
;     __device__ __forceinline__ void operator()(const f32x4 (&acc)[2][2][4][2], const Unit& u, int wr, int wc, int fr, int fq) const {
;     ...
;         for (int ai = 0; ai < 2; ++ai)
; #pragma unroll
;             for (int m = 0; m < 4; ++m) { const size_t ro = (size_t)(row0 + ai * HALF + m * 16) * D + col0;
; #pragma unroll
;                 for (int bj = 0; bj < 2; ++bj) { const u32x4 h = *(const u32x4*)(hb + ro + bj * HALF); const f32x4 v0 = acc[ai][bj][m][0], v1 = acc[ai][bj][m][1];
;                     u32x4 w; w.x = cvt_pk_bf16(v0[0] + ALPHA * bflo(h.x), v0[1] + ALPHA * bfhi(h.x)); w.y = cvt_pk_bf16(v0[2] + ALPHA * bflo(h.y), v0[3] + ALPHA * bfhi(h.y));
;                     w.z = cvt_pk_bf16(v1[0] + ALPHA * bflo(h.z), v1[1] + ALPHA * bfhi(h.z)); w.w = cvt_pk_bf16(v1[2] + ALPHA * bflo(h.w), v1[3] + ALPHA * bfhi(h.w));
;                     *(u32x4*)(Z + ro + bj * HALF) = w; } }
	v_lshlrev_b32_e32 v134, 16, v152
	v_and_b32_e32 v135, 0xffff0000, v152
	v_pk_fma_f32 v[134:135], v[134:135], s[88:89], v[54:55] op_sel_hi:[1,0,1]
	s_nop 0
	v_cvt_pk_bf16_f32 v152, v134, v135
	v_lshlrev_b32_e32 v134, 16, v153
	v_and_b32_e32 v135, 0xffff0000, v153
	v_pk_fma_f32 v[134:135], v[134:135], s[88:89], v[56:57] op_sel_hi:[1,0,1]
	s_nop 0
	v_cvt_pk_bf16_f32 v153, v134, v135
	v_lshlrev_b32_e32 v134, 16, v154
	v_and_b32_e32 v135, 0xffff0000, v154
	v_pk_fma_f32 v[134:135], v[134:135], s[88:89], v[50:51] op_sel_hi:[1,0,1]
	s_nop 0
	v_cvt_pk_bf16_f32 v154, v134, v135
	v_lshlrev_b32_e32 v134, 16, v155
	v_and_b32_e32 v135, 0xffff0000, v155
	v_pk_fma_f32 v[134:135], v[134:135], s[88:89], v[52:53] op_sel_hi:[1,0,1]
	s_nop 0
	v_cvt_pk_bf16_f32 v155, v134, v135
	global_store_dwordx4 v[140:141], v[152:155], off
	s_nop 1
	s_waitcnt vmcnt(11)
	v_lshlrev_b32_e32 v134, 16, v156
	v_and_b32_e32 v135, 0xffff0000, v156
	v_pk_fma_f32 v[134:135], v[134:135], s[88:89], v[30:31] op_sel_hi:[1,0,1]
	s_nop 0
	v_cvt_pk_bf16_f32 v156, v134, v135
	v_lshlrev_b32_e32 v134, 16, v157
	v_and_b32_e32 v135, 0xffff0000, v157
	v_pk_fma_f32 v[134:135], v[134:135], s[88:89], v[32:33] op_sel_hi:[1,0,1]
	s_nop 0
	v_cvt_pk_bf16_f32 v157, v134, v135
	v_lshlrev_b32_e32 v134, 16, v158
	v_and_b32_e32 v135, 0xffff0000, v158
	v_pk_fma_f32 v[134:135], v[134:135], s[88:89], v[22:23] op_sel_hi:[1,0,1]
	s_nop 0
	v_cvt_pk_bf16_f32 v158, v134, v135
	v_lshlrev_b32_e32 v134, 16, v159
	v_and_b32_e32 v135, 0xffff0000, v159
	v_pk_fma_f32 v[134:135], v[134:135], s[88:89], v[24:25] op_sel_hi:[1,0,1]
	s_nop 0
	v_cvt_pk_bf16_f32 v159, v134, v135
	global_store_dwordx4 v[140:141], v[156:159], off offset:256
	v_add_co_u32_e32 v140, vcc, 0x8000, v140
	s_nop 1
	v_addc_co_u32_e32 v141, vcc, 0, v141, vcc
	s_waitcnt vmcnt(10)
	v_lshlrev_b32_e32 v134, 16, v160
	v_and_b32_e32 v135, 0xffff0000, v160
	v_pk_fma_f32 v[134:135], v[134:135], s[88:89], v[42:43] op_sel_hi:[1,0,1]
	s_nop 0
	v_cvt_pk_bf16_f32 v160, v134, v135
	v_lshlrev_b32_e32 v134, 16, v161
	v_and_b32_e32 v135, 0xffff0000, v161
	v_pk_fma_f32 v[134:135], v[134:135], s[88:89], v[44:45] op_sel_hi:[1,0,1]
	s_nop 0
	v_cvt_pk_bf16_f32 v161, v134, v135
	v_lshlrev_b32_e32 v134, 16, v162
	v_and_b32_e32 v135, 0xffff0000, v162
	v_pk_fma_f32 v[134:135], v[134:135], s[88:89], v[34:35] op_sel_hi:[1,0,1]
	s_nop 0
	v_cvt_pk_bf16_f32 v162, v134, v135
	v_lshlrev_b32_e32 v134, 16, v163
	v_and_b32_e32 v135, 0xffff0000, v163
	v_pk_fma_f32 v[134:135], v[134:135], s[88:89], v[36:37] op_sel_hi:[1,0,1]
	s_nop 0
	v_cvt_pk_bf16_f32 v163, v134, v135
	global_store_dwordx4 v[140:141], v[160:163], off
	s_nop 1
	s_waitcnt vmcnt(9)
	v_lshlrev_b32_e32 v134, 16, v164
	v_and_b32_e32 v135, 0xffff0000, v164
	v_pk_fma_f32 v[134:135], v[134:135], s[88:89], v[14:15] op_sel_hi:[1,0,1]
	s_nop 0
	v_cvt_pk_bf16_f32 v164, v134, v135
	v_lshlrev_b32_e32 v134, 16, v165
	v_and_b32_e32 v135, 0xffff0000, v165
	v_pk_fma_f32 v[134:135], v[134:135], s[88:89], v[16:17] op_sel_hi:[1,0,1]
	s_nop 0
	v_cvt_pk_bf16_f32 v165, v134, v135
	v_lshlrev_b32_e32 v134, 16, v166
	v_and_b32_e32 v135, 0xffff0000, v166
	v_pk_fma_f32 v[134:135], v[134:135], s[88:89], v[10:11] op_sel_hi:[1,0,1]
	s_nop 0
	v_cvt_pk_bf16_f32 v166, v134, v135
	v_lshlrev_b32_e32 v134, 16, v167
	v_and_b32_e32 v135, 0xffff0000, v167
	v_pk_fma_f32 v[134:135], v[134:135], s[88:89], v[12:13] op_sel_hi:[1,0,1]
	s_nop 0
	v_cvt_pk_bf16_f32 v167, v134, v135
	global_store_dwordx4 v[140:141], v[164:167], off offset:256
	v_add_co_u32_e32 v140, vcc, 0x8000, v140
	s_nop 1
	v_addc_co_u32_e32 v141, vcc, 0, v141, vcc
	s_waitcnt vmcnt(8)
	v_lshlrev_b32_e32 v134, 16, v168
	v_and_b32_e32 v135, 0xffff0000, v168
	v_pk_fma_f32 v[134:135], v[134:135], s[88:89], v[26:27] op_sel_hi:[1,0,1]
	s_nop 0
	v_cvt_pk_bf16_f32 v168, v134, v135
	v_lshlrev_b32_e32 v134, 16, v169
	v_and_b32_e32 v135, 0xffff0000, v169
	v_pk_fma_f32 v[134:135], v[134:135], s[88:89], v[28:29] op_sel_hi:[1,0,1]
	s_nop 0
	v_cvt_pk_bf16_f32 v169, v134, v135
	v_lshlrev_b32_e32 v134, 16, v170
	v_and_b32_e32 v135, 0xffff0000, v170
	v_pk_fma_f32 v[134:135], v[134:135], s[88:89], v[18:19] op_sel_hi:[1,0,1]
	s_nop 0
	v_cvt_pk_bf16_f32 v170, v134, v135
	v_lshlrev_b32_e32 v134, 16, v171
	v_and_b32_e32 v135, 0xffff0000, v171
	v_pk_fma_f32 v[134:135], v[134:135], s[88:89], v[20:21] op_sel_hi:[1,0,1]
	s_nop 0
	v_cvt_pk_bf16_f32 v171, v134, v135
	global_store_dwordx4 v[140:141], v[168:171], off
	s_nop 1
	s_waitcnt vmcnt(7)
	v_lshlrev_b32_e32 v134, 16, v172
	v_and_b32_e32 v135, 0xffff0000, v172
	v_pk_fma_f32 v[134:135], v[134:135], s[88:89], v[6:7] op_sel_hi:[1,0,1]
	s_nop 0
	v_cvt_pk_bf16_f32 v172, v134, v135
	v_lshlrev_b32_e32 v134, 16, v173
	v_and_b32_e32 v135, 0xffff0000, v173
	v_pk_fma_f32 v[134:135], v[134:135], s[88:89], v[8:9] op_sel_hi:[1,0,1]
	s_nop 0
	v_cvt_pk_bf16_f32 v173, v134, v135
	v_lshlrev_b32_e32 v134, 16, v174
	v_and_b32_e32 v135, 0xffff0000, v174
	v_pk_fma_f32 v[134:135], v[134:135], s[88:89], v[2:3] op_sel_hi:[1,0,1]
	s_nop 0
	v_cvt_pk_bf16_f32 v174, v134, v135
	v_lshlrev_b32_e32 v134, 16, v175
	v_and_b32_e32 v135, 0xffff0000, v175
	v_pk_fma_f32 v[134:135], v[134:135], s[88:89], v[4:5] op_sel_hi:[1,0,1]
	s_nop 0
	v_cvt_pk_bf16_f32 v175, v134, v135
	global_store_dwordx4 v[140:141], v[172:175], off offset:256
	s_nop 1
	s_mov_b64 s[22:23], 0
	s_branch .LBB0_1009
;     __device__ __forceinline__ void operator()(const f32x4 (&acc)[2][2][4][2], const Unit& u, int wr, int wc, int fr, int fq) const {
;     ...
;         if (u.kt * BK < Kfull) {
;             float* zp = ZP + ((size_t)u.e * BM + (wr * 64 + fr)) * D + col0;
; #pragma unroll
;             for (int ai = 0; ai < 2; ++ai)
; #pragma unroll
;                 for (int m = 0; m < 4; ++m)
; #pragma unroll
;                     for (int bj = 0; bj < 2; ++bj) { float* q = zp + (size_t)(ai * HALF + m * 16) * D + bj * HALF; *(f32x4*)q = acc[ai][bj][m][0]; *(f32x4*)(q + 4) = acc[ai][bj][m][1]; }
;             return;
.Lgo_ks:
	s_barrier
.LBB0_1009:
	s_andn2_b64 vcc, exec, s[22:23]
	s_cbranch_vccnz .LBB0_987
	s_ashr_i32 s9, s8, 31
	s_lshl_b64 s[8:9], s[8:9], 20
	v_lshl_add_u64 v[132:133], v[190:191], 0, s[8:9]
	v_lshl_add_u64 v[130:131], v[130:131], 2, v[132:133]
	global_store_dwordx4 v[130:131], v[126:129], off
	global_store_dwordx4 v[130:131], v[122:125], off offset:16
	global_store_dwordx4 v[130:131], v[94:97], off offset:512
	global_store_dwordx4 v[130:131], v[90:93], off offset:528
	s_mov_b32 s8, 0x80000
	s_nop 0
	v_add_co_u32_e32 v90, vcc, 0x10000, v130
	s_nop 1
	v_addc_co_u32_e32 v91, vcc, 0, v131, vcc
	global_store_dwordx4 v[90:91], v[118:121], off
	global_store_dwordx4 v[90:91], v[114:117], off offset:16
	global_store_dwordx4 v[90:91], v[86:89], off offset:512
	global_store_dwordx4 v[90:91], v[82:85], off offset:528
	s_nop 1
	v_add_co_u32_e32 v82, vcc, 0x20000, v130
	s_nop 1
	v_addc_co_u32_e32 v83, vcc, 0, v131, vcc
	global_store_dwordx4 v[82:83], v[110:113], off
	global_store_dwordx4 v[82:83], v[106:109], off offset:16
	global_store_dwordx4 v[82:83], v[78:81], off offset:512
	global_store_dwordx4 v[82:83], v[74:77], off offset:528
	s_nop 1
	v_add_co_u32_e32 v74, vcc, 0x30000, v130
	s_nop 1
	v_addc_co_u32_e32 v75, vcc, 0, v131, vcc
	global_store_dwordx4 v[74:75], v[102:105], off
	global_store_dwordx4 v[74:75], v[98:101], off offset:16
	global_store_dwordx4 v[74:75], v[70:73], off offset:512
	global_store_dwordx4 v[74:75], v[66:69], off offset:528
	s_nop 1
	v_add_co_u32_e32 v66, vcc, s8, v130
	s_nop 1
	v_addc_co_u32_e32 v67, vcc, 0, v131, vcc
	global_store_dwordx4 v[66:67], v[62:65], off
	global_store_dwordx4 v[66:67], v[58:61], off offset:16
	global_store_dwordx4 v[66:67], v[46:49], off offset:512
	global_store_dwordx4 v[66:67], v[38:41], off offset:528
	s_nop 1
	v_add_co_u32_e32 v38, vcc, 0x90000, v130
	s_nop 1
	v_addc_co_u32_e32 v39, vcc, 0, v131, vcc
	global_store_dwordx4 v[38:39], v[54:57], off
	global_store_dwordx4 v[38:39], v[50:53], off offset:16
	global_store_dwordx4 v[38:39], v[30:33], off offset:512
	global_store_dwordx4 v[38:39], v[22:25], off offset:528
	s_nop 1
	v_add_co_u32_e32 v22, vcc, 0xa0000, v130
	s_nop 1
	v_addc_co_u32_e32 v23, vcc, 0, v131, vcc
	global_store_dwordx4 v[22:23], v[42:45], off
	global_store_dwordx4 v[22:23], v[34:37], off offset:16
	global_store_dwordx4 v[22:23], v[14:17], off offset:512
	global_store_dwordx4 v[22:23], v[10:13], off offset:528
	s_nop 1
	v_add_co_u32_e32 v10, vcc, 0xb0000, v130
	s_nop 1
	v_addc_co_u32_e32 v11, vcc, 0, v131, vcc
	global_store_dwordx4 v[10:11], v[26:29], off
	global_store_dwordx4 v[10:11], v[18:21], off offset:16
	global_store_dwordx4 v[10:11], v[6:9], off offset:512
	global_store_dwordx4 v[10:11], v[2:5], off offset:528
	s_branch .LBB0_987
